# expert-choice top-k: hand-written radix-select passes (values kept in registers, 16 lane-group histogram copies per bin, DPP bin scan) replace hipcc's pass loops (on top of v27)
# speedup vs baseline: 1.0049x; 1.0049x over previous
.LBB0_1477:
	s_and_b64 s[14:15], s[30:31], exec
	s_cselect_b32 s35, s81, 0x100
	s_cselect_b32 s46, 0x400, 32
	s_mov_b32 s45, 0
	v_and_b32_e32 v7, 63, v6
	v_and_b32_e32 v8, 15, v6
	v_lshlrev_b32_e32 v8, 2, v8
	v_add_u32_e32 v16, 0x9000, v8
	v_add_u32_e32 v17, 0xd000, v8
	v_lshl_add_u32 v18, v6, 2, 64
	v_lshlrev_b32_e32 v19, 5, v6
	v_add_u32_e32 v19, 0x9000, v19
	v_mov_b32_e32 v20, 0
	v_mov_b32_e32 v21, 0
	v_mov_b32_e32 v22, 0
	v_mov_b32_e32 v23, 0
	ds_write_b128 v19, v[20:23]
	ds_write_b128 v19, v[20:23] offset:16
	s_waitcnt lgkmcnt(0)
	s_barrier
	v_cmp_gt_i32_e32 vcc, s35, v6
	s_and_saveexec_b64 s[40:41], vcc
	s_cbranch_execz .Ltk_p0_hd
	ds_read_b32 v32, v18
	s_and_b64 s[14:15], s[30:31], exec
	s_cbranch_scc0 .Ltk_ld_done
	ds_read_b32 v33, v18 offset:2048
	ds_read_b32 v34, v18 offset:4096
	ds_read_b32 v35, v18 offset:6144
	ds_read_b32 v36, v18 offset:8192
	ds_read_b32 v37, v18 offset:10240
	ds_read_b32 v38, v18 offset:12288
	ds_read_b32 v39, v18 offset:14336
	ds_read_b32 v40, v18 offset:16384
	ds_read_b32 v41, v18 offset:18432
	ds_read_b32 v42, v18 offset:20480
	ds_read_b32 v43, v18 offset:22528
	ds_read_b32 v44, v18 offset:24576
	ds_read_b32 v45, v18 offset:26624
	ds_read_b32 v46, v18 offset:28672
	ds_read_b32 v47, v18 offset:30720
.Ltk_ld_done:
	s_waitcnt lgkmcnt(0)
	v_bfe_u32 v9, v32, 24, 8
	v_lshl_add_u32 v9, v9, 6, v16
	ds_add_u32 v9, v220
	s_and_b64 s[14:15], s[30:31], exec
	s_cbranch_scc0 .Ltk_p0_hd
	v_bfe_u32 v9, v33, 24, 8
	v_lshl_add_u32 v9, v9, 6, v16
	ds_add_u32 v9, v220
	v_bfe_u32 v9, v34, 24, 8
	v_lshl_add_u32 v9, v9, 6, v16
	ds_add_u32 v9, v220
	v_bfe_u32 v9, v35, 24, 8
	v_lshl_add_u32 v9, v9, 6, v16
	ds_add_u32 v9, v220
	v_bfe_u32 v9, v36, 24, 8
	v_lshl_add_u32 v9, v9, 6, v16
	ds_add_u32 v9, v220
	v_bfe_u32 v9, v37, 24, 8
	v_lshl_add_u32 v9, v9, 6, v16
	ds_add_u32 v9, v220
	v_bfe_u32 v9, v38, 24, 8
	v_lshl_add_u32 v9, v9, 6, v16
	ds_add_u32 v9, v220
	v_bfe_u32 v9, v39, 24, 8
	v_lshl_add_u32 v9, v9, 6, v16
	ds_add_u32 v9, v220
	v_bfe_u32 v9, v40, 24, 8
	v_lshl_add_u32 v9, v9, 6, v16
	ds_add_u32 v9, v220
	v_bfe_u32 v9, v41, 24, 8
	v_lshl_add_u32 v9, v9, 6, v16
	ds_add_u32 v9, v220
	v_bfe_u32 v9, v42, 24, 8
	v_lshl_add_u32 v9, v9, 6, v16
	ds_add_u32 v9, v220
	v_bfe_u32 v9, v43, 24, 8
	v_lshl_add_u32 v9, v9, 6, v16
	ds_add_u32 v9, v220
	v_bfe_u32 v9, v44, 24, 8
	v_lshl_add_u32 v9, v9, 6, v16
	ds_add_u32 v9, v220
	v_bfe_u32 v9, v45, 24, 8
	v_lshl_add_u32 v9, v9, 6, v16
	ds_add_u32 v9, v220
	v_bfe_u32 v9, v46, 24, 8
	v_lshl_add_u32 v9, v9, 6, v16
	ds_add_u32 v9, v220
	v_bfe_u32 v9, v47, 24, 8
	v_lshl_add_u32 v9, v9, 6, v16
	ds_add_u32 v9, v220
.Ltk_p0_hd:
	s_mov_b64 exec, s[40:41]
	s_waitcnt lgkmcnt(0)
	s_barrier
	v_cmp_gt_u32_e32 vcc, 64, v6
	s_and_saveexec_b64 s[40:41], vcc
	s_cbranch_execz .Ltk_p0_sd
	v_lshlrev_b32_e32 v8, 8, v7
	v_sub_u32_e32 v8, 0xcf00, v8
	ds_read_b128 v[48:51], v8 offset:0
	ds_read_b128 v[52:55], v8 offset:16
	ds_read_b128 v[56:59], v8 offset:32
	ds_read_b128 v[60:63], v8 offset:48
	ds_read_b128 v[64:67], v8 offset:64
	ds_read_b128 v[68:71], v8 offset:80
	ds_read_b128 v[72:75], v8 offset:96
	ds_read_b128 v[76:79], v8 offset:112
	ds_read_b128 v[80:83], v8 offset:128
	ds_read_b128 v[84:87], v8 offset:144
	ds_read_b128 v[88:91], v8 offset:160
	ds_read_b128 v[92:95], v8 offset:176
	ds_read_b128 v[96:99], v8 offset:192
	ds_read_b128 v[100:103], v8 offset:208
	ds_read_b128 v[104:107], v8 offset:224
	ds_read_b128 v[108:111], v8 offset:240
	s_waitcnt lgkmcnt(0)
	v_add3_u32 v27, v48, v49, v50
	v_add3_u32 v27, v27, v51, v52
	v_add3_u32 v27, v27, v53, v54
	v_add3_u32 v27, v27, v55, v56
	v_add3_u32 v27, v27, v57, v58
	v_add3_u32 v27, v27, v59, v60
	v_add3_u32 v27, v27, v61, v62
	v_add_u32_e32 v27, v27, v63
	v_add3_u32 v26, v64, v65, v66
	v_add3_u32 v26, v26, v67, v68
	v_add3_u32 v26, v26, v69, v70
	v_add3_u32 v26, v26, v71, v72
	v_add3_u32 v26, v26, v73, v74
	v_add3_u32 v26, v26, v75, v76
	v_add3_u32 v26, v26, v77, v78
	v_add_u32_e32 v26, v26, v79
	v_add3_u32 v25, v80, v81, v82
	v_add3_u32 v25, v25, v83, v84
	v_add3_u32 v25, v25, v85, v86
	v_add3_u32 v25, v25, v87, v88
	v_add3_u32 v25, v25, v89, v90
	v_add3_u32 v25, v25, v91, v92
	v_add3_u32 v25, v25, v93, v94
	v_add_u32_e32 v25, v25, v95
	v_add3_u32 v24, v96, v97, v98
	v_add3_u32 v24, v24, v99, v100
	v_add3_u32 v24, v24, v101, v102
	v_add3_u32 v24, v24, v103, v104
	v_add3_u32 v24, v24, v105, v106
	v_add3_u32 v24, v24, v107, v108
	v_add3_u32 v24, v24, v109, v110
	v_add_u32_e32 v24, v24, v111
	v_add3_u32 v28, v24, v25, v26
	v_add_u32_e32 v28, v28, v27
	v_mov_b32_e32 v29, v28
	s_nop 1
	v_add_u32_dpp v29, v29, v29 row_shr:1 row_mask:0xf bank_mask:0xf
	s_nop 1
	v_add_u32_dpp v29, v29, v29 row_shr:2 row_mask:0xf bank_mask:0xf
	s_nop 1
	v_add_u32_dpp v29, v29, v29 row_shr:4 row_mask:0xf bank_mask:0xf
	s_nop 1
	v_add_u32_dpp v29, v29, v29 row_shr:8 row_mask:0xf bank_mask:0xf
	s_nop 1
	v_add_u32_dpp v29, v29, v29 row_bcast:15 row_mask:0xa bank_mask:0xf
	s_nop 1
	v_add_u32_dpp v29, v29, v29 row_bcast:31 row_mask:0xc bank_mask:0xf
	s_nop 1
	v_sub_u32_e32 v30, v29, v28
	v_cmp_gt_u32_e64 s[0:1], s46, v30
	v_cmp_le_u32_e64 s[14:15], s46, v29
	s_and_b64 s[0:1], s[0:1], s[14:15]
	s_and_b64 exec, exec, s[0:1]
	s_cbranch_execz .Ltk_p0_sd
	v_lshlrev_b32_e32 v10, 2, v7
	v_sub_u32_e32 v10, 0xff, v10
	v_add_u32_e32 v12, v30, v24
	v_add_u32_e32 v13, v12, v25
	v_add_u32_e32 v14, v13, v26
	v_mov_b32_e32 v11, v30
	v_cmp_gt_u32_e64 s[0:1], s46, v12
	v_cmp_gt_u32_e64 s[14:15], s46, v13
	v_cmp_gt_u32_e64 s[42:43], s46, v14
	s_and_b64 s[14:15], s[14:15], s[0:1]
	s_and_b64 s[42:43], s[42:43], s[14:15]
	s_nop 1
	v_cndmask_b32_e64 v15, 0, 1, s[0:1]
	v_cndmask_b32_e64 v11, v11, v12, s[0:1]
	v_sub_u32_e32 v10, v10, v15
	v_cndmask_b32_e64 v15, 0, 1, s[14:15]
	v_cndmask_b32_e64 v11, v11, v13, s[14:15]
	v_sub_u32_e32 v10, v10, v15
	v_cndmask_b32_e64 v15, 0, 1, s[42:43]
	v_cndmask_b32_e64 v11, v11, v14, s[42:43]
	v_sub_u32_e32 v10, v10, v15
	v_lshlrev_b32_e32 v10, 24, v10
	v_or_b32_e32 v10, s45, v10
	v_sub_u32_e32 v11, s46, v11
	ds_write_b64 v195, v[10:11] offset:33856
.Ltk_p0_sd:
	s_mov_b64 exec, s[40:41]
	s_waitcnt lgkmcnt(0)
	s_barrier
	ds_read_b64 v[10:11], v195 offset:33856
	s_waitcnt lgkmcnt(0)
	v_readfirstlane_b32 s45, v10
	v_readfirstlane_b32 s46, v11
	ds_write_b128 v19, v[20:23]
	ds_write_b128 v19, v[20:23] offset:16
	s_waitcnt lgkmcnt(0)
	s_barrier
	v_cmp_gt_i32_e32 vcc, s35, v6
	s_and_saveexec_b64 s[40:41], vcc
	s_cbranch_execz .Ltk_p1_hd
	v_and_b32_e32 v8, 0xff000000, v32
	v_cmp_eq_u32_e32 vcc, s45, v8
	v_bfe_u32 v9, v32, 16, 8
	v_lshl_add_u32 v9, v9, 6, v16
	s_nop 0
	v_cndmask_b32_e32 v9, v17, v9, vcc
	ds_add_u32 v9, v220
	s_and_b64 s[14:15], s[30:31], exec
	s_cbranch_scc0 .Ltk_p1_hd
	v_and_b32_e32 v8, 0xff000000, v33
	v_cmp_eq_u32_e32 vcc, s45, v8
	v_bfe_u32 v9, v33, 16, 8
	v_lshl_add_u32 v9, v9, 6, v16
	s_nop 0
	v_cndmask_b32_e32 v9, v17, v9, vcc
	ds_add_u32 v9, v220
	v_and_b32_e32 v8, 0xff000000, v34
	v_cmp_eq_u32_e32 vcc, s45, v8
	v_bfe_u32 v9, v34, 16, 8
	v_lshl_add_u32 v9, v9, 6, v16
	s_nop 0
	v_cndmask_b32_e32 v9, v17, v9, vcc
	ds_add_u32 v9, v220
	v_and_b32_e32 v8, 0xff000000, v35
	v_cmp_eq_u32_e32 vcc, s45, v8
	v_bfe_u32 v9, v35, 16, 8
	v_lshl_add_u32 v9, v9, 6, v16
	s_nop 0
	v_cndmask_b32_e32 v9, v17, v9, vcc
	ds_add_u32 v9, v220
	v_and_b32_e32 v8, 0xff000000, v36
	v_cmp_eq_u32_e32 vcc, s45, v8
	v_bfe_u32 v9, v36, 16, 8
	v_lshl_add_u32 v9, v9, 6, v16
	s_nop 0
	v_cndmask_b32_e32 v9, v17, v9, vcc
	ds_add_u32 v9, v220
	v_and_b32_e32 v8, 0xff000000, v37
	v_cmp_eq_u32_e32 vcc, s45, v8
	v_bfe_u32 v9, v37, 16, 8
	v_lshl_add_u32 v9, v9, 6, v16
	s_nop 0
	v_cndmask_b32_e32 v9, v17, v9, vcc
	ds_add_u32 v9, v220
	v_and_b32_e32 v8, 0xff000000, v38
	v_cmp_eq_u32_e32 vcc, s45, v8
	v_bfe_u32 v9, v38, 16, 8
	v_lshl_add_u32 v9, v9, 6, v16
	s_nop 0
	v_cndmask_b32_e32 v9, v17, v9, vcc
	ds_add_u32 v9, v220
	v_and_b32_e32 v8, 0xff000000, v39
	v_cmp_eq_u32_e32 vcc, s45, v8
	v_bfe_u32 v9, v39, 16, 8
	v_lshl_add_u32 v9, v9, 6, v16
	s_nop 0
	v_cndmask_b32_e32 v9, v17, v9, vcc
	ds_add_u32 v9, v220
	v_and_b32_e32 v8, 0xff000000, v40
	v_cmp_eq_u32_e32 vcc, s45, v8
	v_bfe_u32 v9, v40, 16, 8
	v_lshl_add_u32 v9, v9, 6, v16
	s_nop 0
	v_cndmask_b32_e32 v9, v17, v9, vcc
	ds_add_u32 v9, v220
	v_and_b32_e32 v8, 0xff000000, v41
	v_cmp_eq_u32_e32 vcc, s45, v8
	v_bfe_u32 v9, v41, 16, 8
	v_lshl_add_u32 v9, v9, 6, v16
	s_nop 0
	v_cndmask_b32_e32 v9, v17, v9, vcc
	ds_add_u32 v9, v220
	v_and_b32_e32 v8, 0xff000000, v42
	v_cmp_eq_u32_e32 vcc, s45, v8
	v_bfe_u32 v9, v42, 16, 8
	v_lshl_add_u32 v9, v9, 6, v16
	s_nop 0
	v_cndmask_b32_e32 v9, v17, v9, vcc
	ds_add_u32 v9, v220
	v_and_b32_e32 v8, 0xff000000, v43
	v_cmp_eq_u32_e32 vcc, s45, v8
	v_bfe_u32 v9, v43, 16, 8
	v_lshl_add_u32 v9, v9, 6, v16
	s_nop 0
	v_cndmask_b32_e32 v9, v17, v9, vcc
	ds_add_u32 v9, v220
	v_and_b32_e32 v8, 0xff000000, v44
	v_cmp_eq_u32_e32 vcc, s45, v8
	v_bfe_u32 v9, v44, 16, 8
	v_lshl_add_u32 v9, v9, 6, v16
	s_nop 0
	v_cndmask_b32_e32 v9, v17, v9, vcc
	ds_add_u32 v9, v220
	v_and_b32_e32 v8, 0xff000000, v45
	v_cmp_eq_u32_e32 vcc, s45, v8
	v_bfe_u32 v9, v45, 16, 8
	v_lshl_add_u32 v9, v9, 6, v16
	s_nop 0
	v_cndmask_b32_e32 v9, v17, v9, vcc
	ds_add_u32 v9, v220
	v_and_b32_e32 v8, 0xff000000, v46
	v_cmp_eq_u32_e32 vcc, s45, v8
	v_bfe_u32 v9, v46, 16, 8
	v_lshl_add_u32 v9, v9, 6, v16
	s_nop 0
	v_cndmask_b32_e32 v9, v17, v9, vcc
	ds_add_u32 v9, v220
	v_and_b32_e32 v8, 0xff000000, v47
	v_cmp_eq_u32_e32 vcc, s45, v8
	v_bfe_u32 v9, v47, 16, 8
	v_lshl_add_u32 v9, v9, 6, v16
	s_nop 0
	v_cndmask_b32_e32 v9, v17, v9, vcc
	ds_add_u32 v9, v220
.Ltk_p1_hd:
	s_mov_b64 exec, s[40:41]
	s_waitcnt lgkmcnt(0)
	s_barrier
	v_cmp_gt_u32_e32 vcc, 64, v6
	s_and_saveexec_b64 s[40:41], vcc
	s_cbranch_execz .Ltk_p1_sd
	v_lshlrev_b32_e32 v8, 8, v7
	v_sub_u32_e32 v8, 0xcf00, v8
	ds_read_b128 v[48:51], v8 offset:0
	ds_read_b128 v[52:55], v8 offset:16
	ds_read_b128 v[56:59], v8 offset:32
	ds_read_b128 v[60:63], v8 offset:48
	ds_read_b128 v[64:67], v8 offset:64
	ds_read_b128 v[68:71], v8 offset:80
	ds_read_b128 v[72:75], v8 offset:96
	ds_read_b128 v[76:79], v8 offset:112
	ds_read_b128 v[80:83], v8 offset:128
	ds_read_b128 v[84:87], v8 offset:144
	ds_read_b128 v[88:91], v8 offset:160
	ds_read_b128 v[92:95], v8 offset:176
	ds_read_b128 v[96:99], v8 offset:192
	ds_read_b128 v[100:103], v8 offset:208
	ds_read_b128 v[104:107], v8 offset:224
	ds_read_b128 v[108:111], v8 offset:240
	s_waitcnt lgkmcnt(0)
	v_add3_u32 v27, v48, v49, v50
	v_add3_u32 v27, v27, v51, v52
	v_add3_u32 v27, v27, v53, v54
	v_add3_u32 v27, v27, v55, v56
	v_add3_u32 v27, v27, v57, v58
	v_add3_u32 v27, v27, v59, v60
	v_add3_u32 v27, v27, v61, v62
	v_add_u32_e32 v27, v27, v63
	v_add3_u32 v26, v64, v65, v66
	v_add3_u32 v26, v26, v67, v68
	v_add3_u32 v26, v26, v69, v70
	v_add3_u32 v26, v26, v71, v72
	v_add3_u32 v26, v26, v73, v74
	v_add3_u32 v26, v26, v75, v76
	v_add3_u32 v26, v26, v77, v78
	v_add_u32_e32 v26, v26, v79
	v_add3_u32 v25, v80, v81, v82
	v_add3_u32 v25, v25, v83, v84
	v_add3_u32 v25, v25, v85, v86
	v_add3_u32 v25, v25, v87, v88
	v_add3_u32 v25, v25, v89, v90
	v_add3_u32 v25, v25, v91, v92
	v_add3_u32 v25, v25, v93, v94
	v_add_u32_e32 v25, v25, v95
	v_add3_u32 v24, v96, v97, v98
	v_add3_u32 v24, v24, v99, v100
	v_add3_u32 v24, v24, v101, v102
	v_add3_u32 v24, v24, v103, v104
	v_add3_u32 v24, v24, v105, v106
	v_add3_u32 v24, v24, v107, v108
	v_add3_u32 v24, v24, v109, v110
	v_add_u32_e32 v24, v24, v111
	v_add3_u32 v28, v24, v25, v26
	v_add_u32_e32 v28, v28, v27
	v_mov_b32_e32 v29, v28
	s_nop 1
	v_add_u32_dpp v29, v29, v29 row_shr:1 row_mask:0xf bank_mask:0xf
	s_nop 1
	v_add_u32_dpp v29, v29, v29 row_shr:2 row_mask:0xf bank_mask:0xf
	s_nop 1
	v_add_u32_dpp v29, v29, v29 row_shr:4 row_mask:0xf bank_mask:0xf
	s_nop 1
	v_add_u32_dpp v29, v29, v29 row_shr:8 row_mask:0xf bank_mask:0xf
	s_nop 1
	v_add_u32_dpp v29, v29, v29 row_bcast:15 row_mask:0xa bank_mask:0xf
	s_nop 1
	v_add_u32_dpp v29, v29, v29 row_bcast:31 row_mask:0xc bank_mask:0xf
	s_nop 1
	v_sub_u32_e32 v30, v29, v28
	v_cmp_gt_u32_e64 s[0:1], s46, v30
	v_cmp_le_u32_e64 s[14:15], s46, v29
	s_and_b64 s[0:1], s[0:1], s[14:15]
	s_and_b64 exec, exec, s[0:1]
	s_cbranch_execz .Ltk_p1_sd
	v_lshlrev_b32_e32 v10, 2, v7
	v_sub_u32_e32 v10, 0xff, v10
	v_add_u32_e32 v12, v30, v24
	v_add_u32_e32 v13, v12, v25
	v_add_u32_e32 v14, v13, v26
	v_mov_b32_e32 v11, v30
	v_cmp_gt_u32_e64 s[0:1], s46, v12
	v_cmp_gt_u32_e64 s[14:15], s46, v13
	v_cmp_gt_u32_e64 s[42:43], s46, v14
	s_and_b64 s[14:15], s[14:15], s[0:1]
	s_and_b64 s[42:43], s[42:43], s[14:15]
	s_nop 1
	v_cndmask_b32_e64 v15, 0, 1, s[0:1]
	v_cndmask_b32_e64 v11, v11, v12, s[0:1]
	v_sub_u32_e32 v10, v10, v15
	v_cndmask_b32_e64 v15, 0, 1, s[14:15]
	v_cndmask_b32_e64 v11, v11, v13, s[14:15]
	v_sub_u32_e32 v10, v10, v15
	v_cndmask_b32_e64 v15, 0, 1, s[42:43]
	v_cndmask_b32_e64 v11, v11, v14, s[42:43]
	v_sub_u32_e32 v10, v10, v15
	v_lshlrev_b32_e32 v10, 16, v10
	v_or_b32_e32 v10, s45, v10
	v_sub_u32_e32 v11, s46, v11
	ds_write_b64 v195, v[10:11] offset:33856
.Ltk_p1_sd:
	s_mov_b64 exec, s[40:41]
	s_waitcnt lgkmcnt(0)
	s_barrier
	ds_read_b64 v[10:11], v195 offset:33856
	s_waitcnt lgkmcnt(0)
	v_readfirstlane_b32 s45, v10
	v_readfirstlane_b32 s46, v11
	ds_write_b128 v19, v[20:23]
	ds_write_b128 v19, v[20:23] offset:16
	s_waitcnt lgkmcnt(0)
	s_barrier
	v_cmp_gt_i32_e32 vcc, s35, v6
	s_and_saveexec_b64 s[40:41], vcc
	s_cbranch_execz .Ltk_p2_hd
	v_and_b32_e32 v8, 0xffff0000, v32
	v_cmp_eq_u32_e32 vcc, s45, v8
	v_bfe_u32 v9, v32, 8, 8
	v_lshl_add_u32 v9, v9, 6, v16
	s_nop 0
	v_cndmask_b32_e32 v9, v17, v9, vcc
	ds_add_u32 v9, v220
	s_and_b64 s[14:15], s[30:31], exec
	s_cbranch_scc0 .Ltk_p2_hd
	v_and_b32_e32 v8, 0xffff0000, v33
	v_cmp_eq_u32_e32 vcc, s45, v8
	v_bfe_u32 v9, v33, 8, 8
	v_lshl_add_u32 v9, v9, 6, v16
	s_nop 0
	v_cndmask_b32_e32 v9, v17, v9, vcc
	ds_add_u32 v9, v220
	v_and_b32_e32 v8, 0xffff0000, v34
	v_cmp_eq_u32_e32 vcc, s45, v8
	v_bfe_u32 v9, v34, 8, 8
	v_lshl_add_u32 v9, v9, 6, v16
	s_nop 0
	v_cndmask_b32_e32 v9, v17, v9, vcc
	ds_add_u32 v9, v220
	v_and_b32_e32 v8, 0xffff0000, v35
	v_cmp_eq_u32_e32 vcc, s45, v8
	v_bfe_u32 v9, v35, 8, 8
	v_lshl_add_u32 v9, v9, 6, v16
	s_nop 0
	v_cndmask_b32_e32 v9, v17, v9, vcc
	ds_add_u32 v9, v220
	v_and_b32_e32 v8, 0xffff0000, v36
	v_cmp_eq_u32_e32 vcc, s45, v8
	v_bfe_u32 v9, v36, 8, 8
	v_lshl_add_u32 v9, v9, 6, v16
	s_nop 0
	v_cndmask_b32_e32 v9, v17, v9, vcc
	ds_add_u32 v9, v220
	v_and_b32_e32 v8, 0xffff0000, v37
	v_cmp_eq_u32_e32 vcc, s45, v8
	v_bfe_u32 v9, v37, 8, 8
	v_lshl_add_u32 v9, v9, 6, v16
	s_nop 0
	v_cndmask_b32_e32 v9, v17, v9, vcc
	ds_add_u32 v9, v220
	v_and_b32_e32 v8, 0xffff0000, v38
	v_cmp_eq_u32_e32 vcc, s45, v8
	v_bfe_u32 v9, v38, 8, 8
	v_lshl_add_u32 v9, v9, 6, v16
	s_nop 0
	v_cndmask_b32_e32 v9, v17, v9, vcc
	ds_add_u32 v9, v220
	v_and_b32_e32 v8, 0xffff0000, v39
	v_cmp_eq_u32_e32 vcc, s45, v8
	v_bfe_u32 v9, v39, 8, 8
	v_lshl_add_u32 v9, v9, 6, v16
	s_nop 0
	v_cndmask_b32_e32 v9, v17, v9, vcc
	ds_add_u32 v9, v220
	v_and_b32_e32 v8, 0xffff0000, v40
	v_cmp_eq_u32_e32 vcc, s45, v8
	v_bfe_u32 v9, v40, 8, 8
	v_lshl_add_u32 v9, v9, 6, v16
	s_nop 0
	v_cndmask_b32_e32 v9, v17, v9, vcc
	ds_add_u32 v9, v220
	v_and_b32_e32 v8, 0xffff0000, v41
	v_cmp_eq_u32_e32 vcc, s45, v8
	v_bfe_u32 v9, v41, 8, 8
	v_lshl_add_u32 v9, v9, 6, v16
	s_nop 0
	v_cndmask_b32_e32 v9, v17, v9, vcc
	ds_add_u32 v9, v220
	v_and_b32_e32 v8, 0xffff0000, v42
	v_cmp_eq_u32_e32 vcc, s45, v8
	v_bfe_u32 v9, v42, 8, 8
	v_lshl_add_u32 v9, v9, 6, v16
	s_nop 0
	v_cndmask_b32_e32 v9, v17, v9, vcc
	ds_add_u32 v9, v220
	v_and_b32_e32 v8, 0xffff0000, v43
	v_cmp_eq_u32_e32 vcc, s45, v8
	v_bfe_u32 v9, v43, 8, 8
	v_lshl_add_u32 v9, v9, 6, v16
	s_nop 0
	v_cndmask_b32_e32 v9, v17, v9, vcc
	ds_add_u32 v9, v220
	v_and_b32_e32 v8, 0xffff0000, v44
	v_cmp_eq_u32_e32 vcc, s45, v8
	v_bfe_u32 v9, v44, 8, 8
	v_lshl_add_u32 v9, v9, 6, v16
	s_nop 0
	v_cndmask_b32_e32 v9, v17, v9, vcc
	ds_add_u32 v9, v220
	v_and_b32_e32 v8, 0xffff0000, v45
	v_cmp_eq_u32_e32 vcc, s45, v8
	v_bfe_u32 v9, v45, 8, 8
	v_lshl_add_u32 v9, v9, 6, v16
	s_nop 0
	v_cndmask_b32_e32 v9, v17, v9, vcc
	ds_add_u32 v9, v220
	v_and_b32_e32 v8, 0xffff0000, v46
	v_cmp_eq_u32_e32 vcc, s45, v8
	v_bfe_u32 v9, v46, 8, 8
	v_lshl_add_u32 v9, v9, 6, v16
	s_nop 0
	v_cndmask_b32_e32 v9, v17, v9, vcc
	ds_add_u32 v9, v220
	v_and_b32_e32 v8, 0xffff0000, v47
	v_cmp_eq_u32_e32 vcc, s45, v8
	v_bfe_u32 v9, v47, 8, 8
	v_lshl_add_u32 v9, v9, 6, v16
	s_nop 0
	v_cndmask_b32_e32 v9, v17, v9, vcc
	ds_add_u32 v9, v220
.Ltk_p2_hd:
	s_mov_b64 exec, s[40:41]
	s_waitcnt lgkmcnt(0)
	s_barrier
	v_cmp_gt_u32_e32 vcc, 64, v6
	s_and_saveexec_b64 s[40:41], vcc
	s_cbranch_execz .Ltk_p2_sd
	v_lshlrev_b32_e32 v8, 8, v7
	v_sub_u32_e32 v8, 0xcf00, v8
	ds_read_b128 v[48:51], v8 offset:0
	ds_read_b128 v[52:55], v8 offset:16
	ds_read_b128 v[56:59], v8 offset:32
	ds_read_b128 v[60:63], v8 offset:48
	ds_read_b128 v[64:67], v8 offset:64
	ds_read_b128 v[68:71], v8 offset:80
	ds_read_b128 v[72:75], v8 offset:96
	ds_read_b128 v[76:79], v8 offset:112
	ds_read_b128 v[80:83], v8 offset:128
	ds_read_b128 v[84:87], v8 offset:144
	ds_read_b128 v[88:91], v8 offset:160
	ds_read_b128 v[92:95], v8 offset:176
	ds_read_b128 v[96:99], v8 offset:192
	ds_read_b128 v[100:103], v8 offset:208
	ds_read_b128 v[104:107], v8 offset:224
	ds_read_b128 v[108:111], v8 offset:240
	s_waitcnt lgkmcnt(0)
	v_add3_u32 v27, v48, v49, v50
	v_add3_u32 v27, v27, v51, v52
	v_add3_u32 v27, v27, v53, v54
	v_add3_u32 v27, v27, v55, v56
	v_add3_u32 v27, v27, v57, v58
	v_add3_u32 v27, v27, v59, v60
	v_add3_u32 v27, v27, v61, v62
	v_add_u32_e32 v27, v27, v63
	v_add3_u32 v26, v64, v65, v66
	v_add3_u32 v26, v26, v67, v68
	v_add3_u32 v26, v26, v69, v70
	v_add3_u32 v26, v26, v71, v72
	v_add3_u32 v26, v26, v73, v74
	v_add3_u32 v26, v26, v75, v76
	v_add3_u32 v26, v26, v77, v78
	v_add_u32_e32 v26, v26, v79
	v_add3_u32 v25, v80, v81, v82
	v_add3_u32 v25, v25, v83, v84
	v_add3_u32 v25, v25, v85, v86
	v_add3_u32 v25, v25, v87, v88
	v_add3_u32 v25, v25, v89, v90
	v_add3_u32 v25, v25, v91, v92
	v_add3_u32 v25, v25, v93, v94
	v_add_u32_e32 v25, v25, v95
	v_add3_u32 v24, v96, v97, v98
	v_add3_u32 v24, v24, v99, v100
	v_add3_u32 v24, v24, v101, v102
	v_add3_u32 v24, v24, v103, v104
	v_add3_u32 v24, v24, v105, v106
	v_add3_u32 v24, v24, v107, v108
	v_add3_u32 v24, v24, v109, v110
	v_add_u32_e32 v24, v24, v111
	v_add3_u32 v28, v24, v25, v26
	v_add_u32_e32 v28, v28, v27
	v_mov_b32_e32 v29, v28
	s_nop 1
	v_add_u32_dpp v29, v29, v29 row_shr:1 row_mask:0xf bank_mask:0xf
	s_nop 1
	v_add_u32_dpp v29, v29, v29 row_shr:2 row_mask:0xf bank_mask:0xf
	s_nop 1
	v_add_u32_dpp v29, v29, v29 row_shr:4 row_mask:0xf bank_mask:0xf
	s_nop 1
	v_add_u32_dpp v29, v29, v29 row_shr:8 row_mask:0xf bank_mask:0xf
	s_nop 1
	v_add_u32_dpp v29, v29, v29 row_bcast:15 row_mask:0xa bank_mask:0xf
	s_nop 1
	v_add_u32_dpp v29, v29, v29 row_bcast:31 row_mask:0xc bank_mask:0xf
	s_nop 1
	v_sub_u32_e32 v30, v29, v28
	v_cmp_gt_u32_e64 s[0:1], s46, v30
	v_cmp_le_u32_e64 s[14:15], s46, v29
	s_and_b64 s[0:1], s[0:1], s[14:15]
	s_and_b64 exec, exec, s[0:1]
	s_cbranch_execz .Ltk_p2_sd
	v_lshlrev_b32_e32 v10, 2, v7
	v_sub_u32_e32 v10, 0xff, v10
	v_add_u32_e32 v12, v30, v24
	v_add_u32_e32 v13, v12, v25
	v_add_u32_e32 v14, v13, v26
	v_mov_b32_e32 v11, v30
	v_cmp_gt_u32_e64 s[0:1], s46, v12
	v_cmp_gt_u32_e64 s[14:15], s46, v13
	v_cmp_gt_u32_e64 s[42:43], s46, v14
	s_and_b64 s[14:15], s[14:15], s[0:1]
	s_and_b64 s[42:43], s[42:43], s[14:15]
	s_nop 1
	v_cndmask_b32_e64 v15, 0, 1, s[0:1]
	v_cndmask_b32_e64 v11, v11, v12, s[0:1]
	v_sub_u32_e32 v10, v10, v15
	v_cndmask_b32_e64 v15, 0, 1, s[14:15]
	v_cndmask_b32_e64 v11, v11, v13, s[14:15]
	v_sub_u32_e32 v10, v10, v15
	v_cndmask_b32_e64 v15, 0, 1, s[42:43]
	v_cndmask_b32_e64 v11, v11, v14, s[42:43]
	v_sub_u32_e32 v10, v10, v15
	v_lshlrev_b32_e32 v10, 8, v10
	v_or_b32_e32 v10, s45, v10
	v_sub_u32_e32 v11, s46, v11
	ds_write_b64 v195, v[10:11] offset:33856
.Ltk_p2_sd:
	s_mov_b64 exec, s[40:41]
	s_waitcnt lgkmcnt(0)
	s_barrier
	ds_read_b64 v[10:11], v195 offset:33856
	s_waitcnt lgkmcnt(0)
	v_readfirstlane_b32 s45, v10
	v_readfirstlane_b32 s46, v11
	ds_write_b128 v19, v[20:23]
	ds_write_b128 v19, v[20:23] offset:16
	s_waitcnt lgkmcnt(0)
	s_barrier
	v_cmp_gt_i32_e32 vcc, s35, v6
	s_and_saveexec_b64 s[40:41], vcc
	s_cbranch_execz .Ltk_p3_hd
	v_and_b32_e32 v8, 0xffffff00, v32
	v_cmp_eq_u32_e32 vcc, s45, v8
	v_bfe_u32 v9, v32, 0, 8
	v_lshl_add_u32 v9, v9, 6, v16
	s_nop 0
	v_cndmask_b32_e32 v9, v17, v9, vcc
	ds_add_u32 v9, v220
	s_and_b64 s[14:15], s[30:31], exec
	s_cbranch_scc0 .Ltk_p3_hd
	v_and_b32_e32 v8, 0xffffff00, v33
	v_cmp_eq_u32_e32 vcc, s45, v8
	v_bfe_u32 v9, v33, 0, 8
	v_lshl_add_u32 v9, v9, 6, v16
	s_nop 0
	v_cndmask_b32_e32 v9, v17, v9, vcc
	ds_add_u32 v9, v220
	v_and_b32_e32 v8, 0xffffff00, v34
	v_cmp_eq_u32_e32 vcc, s45, v8
	v_bfe_u32 v9, v34, 0, 8
	v_lshl_add_u32 v9, v9, 6, v16
	s_nop 0
	v_cndmask_b32_e32 v9, v17, v9, vcc
	ds_add_u32 v9, v220
	v_and_b32_e32 v8, 0xffffff00, v35
	v_cmp_eq_u32_e32 vcc, s45, v8
	v_bfe_u32 v9, v35, 0, 8
	v_lshl_add_u32 v9, v9, 6, v16
	s_nop 0
	v_cndmask_b32_e32 v9, v17, v9, vcc
	ds_add_u32 v9, v220
	v_and_b32_e32 v8, 0xffffff00, v36
	v_cmp_eq_u32_e32 vcc, s45, v8
	v_bfe_u32 v9, v36, 0, 8
	v_lshl_add_u32 v9, v9, 6, v16
	s_nop 0
	v_cndmask_b32_e32 v9, v17, v9, vcc
	ds_add_u32 v9, v220
	v_and_b32_e32 v8, 0xffffff00, v37
	v_cmp_eq_u32_e32 vcc, s45, v8
	v_bfe_u32 v9, v37, 0, 8
	v_lshl_add_u32 v9, v9, 6, v16
	s_nop 0
	v_cndmask_b32_e32 v9, v17, v9, vcc
	ds_add_u32 v9, v220
	v_and_b32_e32 v8, 0xffffff00, v38
	v_cmp_eq_u32_e32 vcc, s45, v8
	v_bfe_u32 v9, v38, 0, 8
	v_lshl_add_u32 v9, v9, 6, v16
	s_nop 0
	v_cndmask_b32_e32 v9, v17, v9, vcc
	ds_add_u32 v9, v220
	v_and_b32_e32 v8, 0xffffff00, v39
	v_cmp_eq_u32_e32 vcc, s45, v8
	v_bfe_u32 v9, v39, 0, 8
	v_lshl_add_u32 v9, v9, 6, v16
	s_nop 0
	v_cndmask_b32_e32 v9, v17, v9, vcc
	ds_add_u32 v9, v220
	v_and_b32_e32 v8, 0xffffff00, v40
	v_cmp_eq_u32_e32 vcc, s45, v8
	v_bfe_u32 v9, v40, 0, 8
	v_lshl_add_u32 v9, v9, 6, v16
	s_nop 0
	v_cndmask_b32_e32 v9, v17, v9, vcc
	ds_add_u32 v9, v220
	v_and_b32_e32 v8, 0xffffff00, v41
	v_cmp_eq_u32_e32 vcc, s45, v8
	v_bfe_u32 v9, v41, 0, 8
	v_lshl_add_u32 v9, v9, 6, v16
	s_nop 0
	v_cndmask_b32_e32 v9, v17, v9, vcc
	ds_add_u32 v9, v220
	v_and_b32_e32 v8, 0xffffff00, v42
	v_cmp_eq_u32_e32 vcc, s45, v8
	v_bfe_u32 v9, v42, 0, 8
	v_lshl_add_u32 v9, v9, 6, v16
	s_nop 0
	v_cndmask_b32_e32 v9, v17, v9, vcc
	ds_add_u32 v9, v220
	v_and_b32_e32 v8, 0xffffff00, v43
	v_cmp_eq_u32_e32 vcc, s45, v8
	v_bfe_u32 v9, v43, 0, 8
	v_lshl_add_u32 v9, v9, 6, v16
	s_nop 0
	v_cndmask_b32_e32 v9, v17, v9, vcc
	ds_add_u32 v9, v220
	v_and_b32_e32 v8, 0xffffff00, v44
	v_cmp_eq_u32_e32 vcc, s45, v8
	v_bfe_u32 v9, v44, 0, 8
	v_lshl_add_u32 v9, v9, 6, v16
	s_nop 0
	v_cndmask_b32_e32 v9, v17, v9, vcc
	ds_add_u32 v9, v220
	v_and_b32_e32 v8, 0xffffff00, v45
	v_cmp_eq_u32_e32 vcc, s45, v8
	v_bfe_u32 v9, v45, 0, 8
	v_lshl_add_u32 v9, v9, 6, v16
	s_nop 0
	v_cndmask_b32_e32 v9, v17, v9, vcc
	ds_add_u32 v9, v220
	v_and_b32_e32 v8, 0xffffff00, v46
	v_cmp_eq_u32_e32 vcc, s45, v8
	v_bfe_u32 v9, v46, 0, 8
	v_lshl_add_u32 v9, v9, 6, v16
	s_nop 0
	v_cndmask_b32_e32 v9, v17, v9, vcc
	ds_add_u32 v9, v220
	v_and_b32_e32 v8, 0xffffff00, v47
	v_cmp_eq_u32_e32 vcc, s45, v8
	v_bfe_u32 v9, v47, 0, 8
	v_lshl_add_u32 v9, v9, 6, v16
	s_nop 0
	v_cndmask_b32_e32 v9, v17, v9, vcc
	ds_add_u32 v9, v220
.Ltk_p3_hd:
	s_mov_b64 exec, s[40:41]
	s_waitcnt lgkmcnt(0)
	s_barrier
	v_cmp_gt_u32_e32 vcc, 64, v6
	s_and_saveexec_b64 s[40:41], vcc
	s_cbranch_execz .Ltk_p3_sd
	v_lshlrev_b32_e32 v8, 8, v7
	v_sub_u32_e32 v8, 0xcf00, v8
	ds_read_b128 v[48:51], v8 offset:0
	ds_read_b128 v[52:55], v8 offset:16
	ds_read_b128 v[56:59], v8 offset:32
	ds_read_b128 v[60:63], v8 offset:48
	ds_read_b128 v[64:67], v8 offset:64
	ds_read_b128 v[68:71], v8 offset:80
	ds_read_b128 v[72:75], v8 offset:96
	ds_read_b128 v[76:79], v8 offset:112
	ds_read_b128 v[80:83], v8 offset:128
	ds_read_b128 v[84:87], v8 offset:144
	ds_read_b128 v[88:91], v8 offset:160
	ds_read_b128 v[92:95], v8 offset:176
	ds_read_b128 v[96:99], v8 offset:192
	ds_read_b128 v[100:103], v8 offset:208
	ds_read_b128 v[104:107], v8 offset:224
	ds_read_b128 v[108:111], v8 offset:240
	s_waitcnt lgkmcnt(0)
	v_add3_u32 v27, v48, v49, v50
	v_add3_u32 v27, v27, v51, v52
	v_add3_u32 v27, v27, v53, v54
	v_add3_u32 v27, v27, v55, v56
	v_add3_u32 v27, v27, v57, v58
	v_add3_u32 v27, v27, v59, v60
	v_add3_u32 v27, v27, v61, v62
	v_add_u32_e32 v27, v27, v63
	v_add3_u32 v26, v64, v65, v66
	v_add3_u32 v26, v26, v67, v68
	v_add3_u32 v26, v26, v69, v70
	v_add3_u32 v26, v26, v71, v72
	v_add3_u32 v26, v26, v73, v74
	v_add3_u32 v26, v26, v75, v76
	v_add3_u32 v26, v26, v77, v78
	v_add_u32_e32 v26, v26, v79
	v_add3_u32 v25, v80, v81, v82
	v_add3_u32 v25, v25, v83, v84
	v_add3_u32 v25, v25, v85, v86
	v_add3_u32 v25, v25, v87, v88
	v_add3_u32 v25, v25, v89, v90
	v_add3_u32 v25, v25, v91, v92
	v_add3_u32 v25, v25, v93, v94
	v_add_u32_e32 v25, v25, v95
	v_add3_u32 v24, v96, v97, v98
	v_add3_u32 v24, v24, v99, v100
	v_add3_u32 v24, v24, v101, v102
	v_add3_u32 v24, v24, v103, v104
	v_add3_u32 v24, v24, v105, v106
	v_add3_u32 v24, v24, v107, v108
	v_add3_u32 v24, v24, v109, v110
	v_add_u32_e32 v24, v24, v111
	v_add3_u32 v28, v24, v25, v26
	v_add_u32_e32 v28, v28, v27
	v_mov_b32_e32 v29, v28
	s_nop 1
	v_add_u32_dpp v29, v29, v29 row_shr:1 row_mask:0xf bank_mask:0xf
	s_nop 1
	v_add_u32_dpp v29, v29, v29 row_shr:2 row_mask:0xf bank_mask:0xf
	s_nop 1
	v_add_u32_dpp v29, v29, v29 row_shr:4 row_mask:0xf bank_mask:0xf
	s_nop 1
	v_add_u32_dpp v29, v29, v29 row_shr:8 row_mask:0xf bank_mask:0xf
	s_nop 1
	v_add_u32_dpp v29, v29, v29 row_bcast:15 row_mask:0xa bank_mask:0xf
	s_nop 1
	v_add_u32_dpp v29, v29, v29 row_bcast:31 row_mask:0xc bank_mask:0xf
	s_nop 1
	v_sub_u32_e32 v30, v29, v28
	v_cmp_gt_u32_e64 s[0:1], s46, v30
	v_cmp_le_u32_e64 s[14:15], s46, v29
	s_and_b64 s[0:1], s[0:1], s[14:15]
	s_and_b64 exec, exec, s[0:1]
	s_cbranch_execz .Ltk_p3_sd
	v_lshlrev_b32_e32 v10, 2, v7
	v_sub_u32_e32 v10, 0xff, v10
	v_add_u32_e32 v12, v30, v24
	v_add_u32_e32 v13, v12, v25
	v_add_u32_e32 v14, v13, v26
	v_mov_b32_e32 v11, v30
	v_cmp_gt_u32_e64 s[0:1], s46, v12
	v_cmp_gt_u32_e64 s[14:15], s46, v13
	v_cmp_gt_u32_e64 s[42:43], s46, v14
	s_and_b64 s[14:15], s[14:15], s[0:1]
	s_and_b64 s[42:43], s[42:43], s[14:15]
	s_nop 1
	v_cndmask_b32_e64 v15, 0, 1, s[0:1]
	v_cndmask_b32_e64 v11, v11, v12, s[0:1]
	v_sub_u32_e32 v10, v10, v15
	v_cndmask_b32_e64 v15, 0, 1, s[14:15]
	v_cndmask_b32_e64 v11, v11, v13, s[14:15]
	v_sub_u32_e32 v10, v10, v15
	v_cndmask_b32_e64 v15, 0, 1, s[42:43]
	v_cndmask_b32_e64 v11, v11, v14, s[42:43]
	v_sub_u32_e32 v10, v10, v15
	v_or_b32_e32 v10, s45, v10
	v_sub_u32_e32 v11, s46, v11
	ds_write_b64 v195, v[10:11] offset:33856
.Ltk_p3_sd:
	s_mov_b64 exec, s[40:41]
	s_mov_b64 s[36:37], exec
	s_branch .LBB0_1525

.LBB0_1495:
	v_ashrrev_i32_e32 v7, 31, v6
	v_lshl_add_u64 v[12:13], v[6:7], 4, s[36:37]
	v_add_co_u32_e32 v8, vcc, 0x2000, v12
	v_lshl_add_u32 v7, v6, 4, 0
	s_nop 0
	v_addc_co_u32_e32 v9, vcc, 0, v13, vcc
	v_add_co_u32_e32 v14, vcc, 0x4000, v12
	global_load_dwordx4 v[2:5], v[12:13], off
	s_nop 0
	global_load_dwordx4 v[8:11], v[8:9], off
	v_addc_co_u32_e32 v15, vcc, 0, v13, vcc
	v_add_co_u32_e32 v16, vcc, 0x6000, v12
	s_nop 1
	v_addc_co_u32_e32 v17, vcc, 0, v13, vcc
	global_load_dwordx4 v[12:15], v[14:15], off
	s_nop 0
	global_load_dwordx4 v[16:19], v[16:17], off
	s_waitcnt vmcnt(3)
	ds_write_b128 v7, v[2:5] offset:64
	s_waitcnt vmcnt(2)
	ds_write_b128 v7, v[8:11] offset:8256
	s_waitcnt vmcnt(1)
	ds_write_b128 v7, v[12:15] offset:16448
	s_waitcnt vmcnt(0)
	ds_write_b128 v7, v[16:19] offset:24640
	s_branch .LBB0_1477
